# p8 + packed f32 adds in the attention halves split into scalar adds
# speedup vs baseline: 1.0170x; 1.0012x over previous
; template <bool FIRST> DEVI bool partialSM(f32x16& p0, f32x16& p1, float& m_reg, float& alpha) {
;     float pmax = p0[0];
; #pragma unroll
;     for (int r = 1; r < 16; ++r) pmax = fmaxf(pmax, p0[r]);
; #pragma unroll
;     for (int r = 0; r < 16; ++r) pmax = fmaxf(pmax, p1[r]);
;     { auto rr = __builtin_amdgcn_permlane32_swap(__float_as_uint(pmax), __float_as_uint(pmax), false, false);
;       pmax = fmaxf(__uint_as_float(rr[0]), __uint_as_float(rr[1])); }
;     if (FIRST) { m_reg = pmax; alpha = 1.f;
; #pragma unroll
;         for (int r = 0; r < 16; ++r) { p0[r] = __builtin_amdgcn_exp2f(p0[r] - pmax); p1[r] = p1[r] - pmax; }
;         return false;
;     } else if (__builtin_expect(__all(pmax <= ATT_THR), 1)) { alpha = 1.f;
; #pragma unroll
;         for (int r = 0; r < 16; ++r) p0[r] = __builtin_amdgcn_exp2f(p0[r]);
;         return false;
;     } else { const float d = fmaxf(pmax, 0.f); alpha = __builtin_amdgcn_exp2f(-d); m_reg += d;
; #pragma unroll
;         for (int r = 0; r < 16; ++r) { p0[r] = __builtin_amdgcn_exp2f(p0[r] - d); p1[r] = p1[r] - d; }
;         return true;
;     }
; }
; DEVI void finishSM(f32x16& p0, f32x16& p1, float alpha, float& l_reg, bf16x8& pa0, bf16x8& pa1, bf16x8& pa2, bf16x8& pa3) {
; #pragma unroll
;     for (int r = 0; r < 16; ++r) p1[r] = __builtin_amdgcn_exp2f(p1[r]);
;     f32x2 s2 = (f32x2){p0[0], p0[1]} + (f32x2){p1[0], p1[1]};
; #pragma unroll
;     for (int r = 2; r < 16; r += 2) s2 += (f32x2){p0[r], p0[r + 1]} + (f32x2){p1[r], p1[r + 1]};
;     float ps = s2[0] + s2[1];
;     { auto rr = __builtin_amdgcn_permlane32_swap(__float_as_uint(ps), __float_as_uint(ps), false, false);
;       ps = __uint_as_float(rr[0]) + __uint_as_float(rr[1]); }
;     l_reg = l_reg * alpha + ps;
;     ...
;     PK4(p0, 0, pa0); PK4(p0, 8, pa1); PK4(p1, 0, pa2); PK4(p1, 8, pa3);
;     ...
; }
; DEVI void qkt(f32x16& p0, f32x16& p1, const char* Kb, const bf16x8 (&qr)[6], int r32, int hi, const f32x16& cinit) {
; #pragma unroll
;     for (int d0 = 0; d0 < 6; ++d0) { const int cb = (d0 * 16 + hi * 8) * 2;
;         const bf16x8 k0 = *(const bf16x8*)(Kb + KSWZ(r32, cb)), k1 = *(const bf16x8*)(Kb + KSWZ(32 + r32, cb));
;         p0 = __builtin_amdgcn_mfma_f32_32x32x16_bf16(k0, qr[d0], d0 == 0 ? cinit : p0, 0, 0, 0);
;         p1 = __builtin_amdgcn_mfma_f32_32x32x16_bf16(k1, qr[d0], d0 == 0 ? cinit : p1, 0, 0, 0); }
; }
.LBB0_696:
	v_add_u32_e32 v174, s98, v204
	v_exp_f32_e32 v66, v66
	v_exp_f32_e32 v67, v67
	s_waitcnt lgkmcnt(1)
	v_mfma_f32_32x32x16_bf16 v[98:113], v[82:85], v[150:153], v[34:49]
	v_add_u32_e32 v82, s98, v184
	v_add_u32_e32 v83, s98, v185
	ds_read_b128 v[208:211], v82 offset:12288
	ds_read_b128 v[212:215], v82 offset:18432
	ds_read_b128 v[216:219], v83 offset:12288
	ds_read_b128 v[220:223], v83 offset:18432
	v_exp_f32_e32 v68, v68
	v_exp_f32_e32 v69, v69
	v_exp_f32_e32 v70, v70
	v_exp_f32_e32 v71, v71
	s_waitcnt lgkmcnt(4)
	v_mfma_f32_32x32x16_bf16 v[82:97], v[124:127], v[150:153], v[34:49]
	ds_read_b128 v[124:127], v174 offset:12288
	ds_read_b128 v[224:227], v174 offset:18432
	v_exp_f32_e32 v72, v72
	v_exp_f32_e32 v73, v73
	v_exp_f32_e32 v74, v74
	v_exp_f32_e32 v75, v75
	v_exp_f32_e32 v76, v76
	v_exp_f32_e32 v77, v77
	s_waitcnt lgkmcnt(5)
	v_mfma_f32_32x32x16_bf16 v[98:113], v[208:211], v[138:141], v[98:113]
	v_add_u32_e32 v174, s98, v205
	v_exp_f32_e32 v78, v78
	v_exp_f32_e32 v79, v79
	ds_read_b128 v[228:231], v174 offset:12288
	ds_read_b128 v[232:235], v174 offset:18432
	v_exp_f32_e32 v80, v80
	v_exp_f32_e32 v81, v81
	v_add_u32_e32 v174, s98, v206
	s_waitcnt lgkmcnt(6)
	v_mfma_f32_32x32x16_bf16 v[82:97], v[212:215], v[138:141], v[82:97]
	v_add_f32_e64 v212, v50, v66
	v_add_f32_e64 v213, v51, v67
	v_add_f32_e64 v214, v52, v68
	v_add_f32_e64 v215, v53, v69
	v_lshl_add_u32 v202, s89, 14, v115
	v_add_f32_e32 v212, v214, v212
	v_add_f32_e32 v213, v215, v213
	v_add_f32_e32 v214, v54, v70
	v_add_f32_e32 v215, v55, v71
	ds_read_b128 v[208:211], v174 offset:12288
	ds_read_b128 v[236:239], v174 offset:18432
	v_add_f32_e32 v212, v214, v212
	v_add_f32_e32 v213, v215, v213
	s_waitcnt lgkmcnt(7)
	v_mfma_f32_32x32x16_bf16 v[98:113], v[216:219], v[134:137], v[98:113]
	v_add_f32_e64 v214, v56, v72
	v_add_f32_e64 v215, v57, v73
	v_cvt_pk_bf16_f32 v50, v50, v51
	v_cvt_pk_bf16_f32 v51, v52, v53
	v_cvt_pk_bf16_f32 v52, v54, v55
	v_cvt_pk_bf16_f32 v53, v56, v57
	v_cvt_pk_bf16_f32 v54, v58, v59
	v_add_f32_e64 v212, v214, v212
	v_add_f32_e64 v213, v215, v213
	s_waitcnt lgkmcnt(6)
	v_mfma_f32_32x32x16_bf16 v[82:97], v[220:223], v[134:137], v[82:97]
	v_add_f32_e64 v214, v58, v74
	v_add_f32_e64 v215, v59, v75
	v_cvt_pk_bf16_f32 v55, v60, v61
	v_cvt_pk_bf16_f32 v56, v62, v63
	v_cvt_pk_bf16_f32 v57, v64, v65
	v_cvt_pk_bf16_f32 v58, v66, v67
	v_cvt_pk_bf16_f32 v59, v68, v69
	v_add_f32_e64 v212, v214, v212
	v_add_f32_e64 v213, v215, v213
	s_waitcnt lgkmcnt(5)
	v_mfma_f32_32x32x16_bf16 v[98:113], v[124:127], v[130:133], v[98:113]
	v_add_f32_e64 v214, v60, v76
	v_add_f32_e64 v215, v61, v77
	v_add_f32_e64 v126, v62, v78
	v_add_f32_e64 v127, v63, v79
	v_add_f32_e64 v124, v214, v212
	v_add_f32_e64 v125, v215, v213
	v_cvt_pk_bf16_f32 v60, v70, v71
	v_cvt_pk_bf16_f32 v61, v72, v73
	v_cvt_pk_bf16_f32 v62, v74, v75
	v_cvt_pk_bf16_f32 v63, v76, v77
	s_waitcnt lgkmcnt(4)
	v_mfma_f32_32x32x16_bf16 v[82:97], v[224:227], v[130:133], v[82:97]
	v_add_f32_e64 v124, v126, v124
	v_add_f32_e64 v125, v127, v125
	v_add_f32_e64 v126, v64, v80
	v_add_f32_e64 v127, v65, v81
	v_cvt_pk_bf16_f32 v64, v78, v79
	v_cvt_pk_bf16_f32 v65, v80, v81
	ds_read_b64_tr_b16 v[66:67], v202 offset:0
	ds_read_b64_tr_b16 v[68:69], v202 offset:0x400
	ds_read_b64_tr_b16 v[70:71], v202 offset:0x800
	s_waitcnt lgkmcnt(6)
	v_mfma_f32_32x32x16_bf16 v[98:113], v[228:231], v[146:149], v[98:113]
	ds_read_b64_tr_b16 v[72:73], v202 offset:0xc00
	ds_read_b64_tr_b16 v[74:75], v202 offset:0x1000
	ds_read_b64_tr_b16 v[76:77], v202 offset:0x1400
	ds_read_b64_tr_b16 v[78:79], v202 offset:0x1800
	ds_read_b64_tr_b16 v[80:81], v202 offset:0x1c00
	v_add_f32_e64 v124, v126, v124
	v_add_f32_e64 v125, v127, v125
	s_waitcnt lgkmcnt(10)
	v_mfma_f32_32x32x16_bf16 v[82:97], v[232:235], v[146:149], v[82:97]
	v_add_f32_e32 v124, v124, v125
	s_nop 0
	v_mov_b32_e32 v125, v124
	s_nop 1
	v_permlane32_swap_b32_e32 v124, v125
	s_waitcnt lgkmcnt(9)
	v_mfma_f32_32x32x16_bf16 v[98:113], v[208:211], v[142:145], v[98:113]
	ds_read_b64_tr_b16 v[208:209], v202 offset:0x200
	ds_read_b64_tr_b16 v[210:211], v202 offset:0x600
	ds_read_b64_tr_b16 v[212:213], v202 offset:0xa00
	ds_read_b64_tr_b16 v[214:215], v202 offset:0xe00
	ds_read_b64_tr_b16 v[216:217], v202 offset:0x1200
	ds_read_b64_tr_b16 v[218:219], v202 offset:0x1600
	ds_read_b64_tr_b16 v[220:221], v202 offset:0x1a00
	s_waitcnt lgkmcnt(15)
	v_mfma_f32_32x32x16_bf16 v[82:97], v[236:239], v[142:145], v[82:97]
	ds_read_b64_tr_b16 v[222:223], v202 offset:0x1e00
	s_waitcnt lgkmcnt(14)
	v_mfma_f32_32x32x16_bf16 v[18:33], v[50:53], v[66:69], v[18:33]
	s_waitcnt lgkmcnt(6)
	v_mfma_f32_32x32x16_bf16 v[2:17], v[50:53], v[208:211], v[2:17]
	s_nop 8
	v_max_f32_e32 v249, v99, v99
	v_max_f32_e32 v250, v98, v98
	v_max_f32_e32 v249, v250, v249
	v_max3_f32 v249, v249, v100, v101
	v_max3_f32 v249, v249, v102, v103
	v_max3_f32 v251, v249, v104, v105
	v_max3_f32 v251, v251, v106, v107
	v_exp_f32_e32 v50, v98
	v_exp_f32_e32 v51, v99
	v_exp_f32_e32 v52, v100
	v_exp_f32_e32 v53, v101
	v_mov_b64_e32 v[66:67], v[82:83]
	v_mov_b64_e32 v[68:69], v[84:85]
	v_mfma_f32_32x32x16_bf16 v[18:33], v[54:57], v[70:73], v[18:33]
	s_waitcnt lgkmcnt(4)
	v_mfma_f32_32x32x16_bf16 v[2:17], v[54:57], v[212:215], v[2:17]
	v_max3_f32 v251, v251, v108, v109
	v_max3_f32 v251, v251, v110, v111
	v_max3_f32 v251, v251, v112, v113
	v_max3_f32 v251, v251, v82, v83
	v_max3_f32 v251, v251, v84, v85
	v_max3_f32 v251, v251, v86, v87
	v_max3_f32 v251, v251, v88, v89
	v_exp_f32_e32 v54, v102
	v_exp_f32_e32 v55, v103
	v_exp_f32_e32 v56, v104
	v_exp_f32_e32 v57, v105
	v_mov_b64_e32 v[70:71], v[86:87]
	v_mov_b64_e32 v[72:73], v[88:89]
	v_mfma_f32_32x32x16_bf16 v[18:33], v[58:61], v[74:77], v[18:33]
	s_waitcnt lgkmcnt(2)
	v_mfma_f32_32x32x16_bf16 v[2:17], v[58:61], v[216:219], v[2:17]
	v_max3_f32 v251, v251, v90, v91
	v_max3_f32 v251, v251, v92, v93
	v_max3_f32 v251, v251, v94, v95
	v_max3_f32 v251, v251, v96, v97
	v_mov_b32_e32 v252, v251
	s_nop 1
	v_permlane32_swap_b32_e32 v251, v252
	v_exp_f32_e32 v58, v106
	v_exp_f32_e32 v59, v107
	v_exp_f32_e32 v60, v108
	v_exp_f32_e32 v61, v109
	v_mov_b64_e32 v[74:75], v[90:91]
	v_mov_b64_e32 v[76:77], v[92:93]
	v_mfma_f32_32x32x16_bf16 v[18:33], v[62:65], v[78:81], v[18:33]
	s_waitcnt lgkmcnt(0)
	v_mfma_f32_32x32x16_bf16 v[2:17], v[62:65], v[220:223], v[2:17]
	v_exp_f32_e32 v62, v110
	v_exp_f32_e32 v63, v111
	v_exp_f32_e32 v64, v112
	v_exp_f32_e32 v65, v113
	v_mov_b64_e32 v[78:79], v[94:95]
	v_mov_b64_e32 v[80:81], v[96:97]
	v_max_f32_e32 v252, v252, v252
	v_max_f32_e32 v251, v251, v251
	v_max_f32_e32 v126, v251, v252
	v_cmp_ge_f32_e32 vcc, s79, v126
	s_cmp_lg_u64 vcc, exec
	s_cselect_b64 s[6:7], -1, 0
	s_cbranch_scc1 .LBB0_705
	v_mov_b32_e32 v208, 1.0
	v_mov_b32_e32 v209, v203
	s_branch .LBB0_699

; #define PK4(P, BASE, OUT) do { u32x4 w = {cvt_pk_bf16(P[BASE + 0], P[BASE + 1]), cvt_pk_bf16(P[BASE + 2], P[BASE + 3]), cvt_pk_bf16(P[BASE + 4], P[BASE + 5]), cvt_pk_bf16(P[BASE + 6], P[BASE + 7])}; \
;     OUT = *reinterpret_cast<bf16x8*>(&w); } while (0)
; DEVI void finishSM(f32x16& p0, f32x16& p1, float alpha, float& l_reg, bf16x8& pa0, bf16x8& pa1, bf16x8& pa2, bf16x8& pa3) {
; #pragma unroll
;     for (int r = 0; r < 16; ++r) p1[r] = __builtin_amdgcn_exp2f(p1[r]);
;     f32x2 s2 = (f32x2){p0[0], p0[1]} + (f32x2){p1[0], p1[1]};
; #pragma unroll
;     for (int r = 2; r < 16; r += 2) s2 += (f32x2){p0[r], p0[r + 1]} + (f32x2){p1[r], p1[r + 1]};
;     float ps = s2[0] + s2[1];
;     { auto rr = __builtin_amdgcn_permlane32_swap(__float_as_uint(ps), __float_as_uint(ps), false, false);
;       ps = __uint_as_float(rr[0]) + __uint_as_float(rr[1]); }
;     l_reg = l_reg * alpha + ps;
;     ...
;     PK4(p0, 0, pa0); PK4(p0, 8, pa1); PK4(p1, 0, pa2); PK4(p1, 8, pa3);
;     ...
; }
; DEVI void qkt(f32x16& p0, f32x16& p1, const char* Kb, const bf16x8 (&qr)[6], int r32, int hi, const f32x16& cinit) {
; #pragma unroll
;     for (int d0 = 0; d0 < 6; ++d0) { const int cb = (d0 * 16 + hi * 8) * 2;
;         const bf16x8 k0 = *(const bf16x8*)(Kb + KSWZ(r32, cb)), k1 = *(const bf16x8*)(Kb + KSWZ(32 + r32, cb));
;         p0 = __builtin_amdgcn_mfma_f32_32x32x16_bf16(k0, qr[d0], d0 == 0 ? cinit : p0, 0, 0, 0);
;         p1 = __builtin_amdgcn_mfma_f32_32x32x16_bf16(k1, qr[d0], d0 == 0 ? cinit : p1, 0, 0, 0); }
; }
.LBB0_702:
	s_mul_i32 s98, s2, 0x6000
	s_add_i32 s98, s96, s98
	s_lshl_b32 s99, s2, 14
	s_add_i32 s99, s97, s99
	s_mul_i32 s6, s61, 0x6000
	s_add_i32 s6, s6, 0
	v_add_u32_e32 v86, s6, v129
	v_lshl_add_u64 v[250:251], v[118:119], 0, s[12:13]
	s_mov_b32 m0, s98
	s_barrier
	ds_read_b128 v[82:85], v86
	ds_read_b128 v[210:213], v86 offset:6144
	global_load_lds_dwordx4 v[250:251], off
	v_exp_f32_e32 v66, v66
	s_waitcnt lgkmcnt(1)
	v_mfma_f32_32x32x16_bf16 v[98:113], v[82:85], v[150:153], v[34:49]
	v_add_u32_e32 v126, s6, v184
	v_lshl_add_u64 v[250:251], v[120:121], 0, s[12:13]
	s_add_i32 m0, s98, 0x2000
	v_exp_f32_e32 v67, v67
	v_exp_f32_e32 v68, v68
	global_load_lds_dwordx4 v[250:251], off
	v_exp_f32_e32 v69, v69
	v_exp_f32_e32 v70, v70
	v_exp_f32_e32 v71, v71
	v_exp_f32_e32 v72, v72
	s_waitcnt lgkmcnt(0)
	v_mfma_f32_32x32x16_bf16 v[82:97], v[210:213], v[150:153], v[34:49]
	ds_read_b128 v[210:213], v126
	ds_read_b128 v[214:217], v126 offset:6144
	v_add_u32_e32 v126, s6, v185
	v_lshl_add_u64 v[250:251], v[122:123], 0, s[12:13]
	s_add_i32 m0, s98, 0x4000
	v_exp_f32_e32 v73, v73
	v_exp_f32_e32 v74, v74
	global_load_lds_dwordx4 v[250:251], off
	v_exp_f32_e32 v75, v75
	v_exp_f32_e32 v76, v76
	v_exp_f32_e32 v77, v77
	s_waitcnt lgkmcnt(1)
	v_mfma_f32_32x32x16_bf16 v[98:113], v[210:213], v[138:141], v[98:113]
	s_mov_b32 m0, s99
	v_exp_f32_e32 v78, v78
	v_exp_f32_e32 v79, v79
	v_lshl_add_u64 v[250:251], v[116:117], 0, s[40:41]
	global_load_lds_dwordx4 v[116:117], off
	s_add_i32 m0, s99, 0x2000
	v_exp_f32_e32 v80, v80
	v_exp_f32_e32 v81, v81
	v_add_u32_e32 v174, 0x2000, v202
	global_load_lds_dwordx4 v[250:251], off
	s_waitcnt lgkmcnt(0)
	v_mfma_f32_32x32x16_bf16 v[82:97], v[214:217], v[138:141], v[82:97]
	ds_read_b128 v[210:213], v126
	ds_read_b128 v[214:217], v126 offset:6144
	v_add_u32_e32 v126, s6, v204
	s_waitcnt lgkmcnt(1)
	v_mfma_f32_32x32x16_bf16 v[98:113], v[210:213], v[134:137], v[98:113]
	ds_read_b128 v[210:213], v126
	ds_read_b128 v[218:221], v126 offset:6144
	v_add_u32_e32 v126, s6, v205
	s_waitcnt lgkmcnt(2)
	v_mfma_f32_32x32x16_bf16 v[82:97], v[214:217], v[134:137], v[82:97]
	ds_read_b128 v[214:217], v126
	ds_read_b128 v[222:225], v126 offset:6144
	v_add_u32_e32 v126, s6, v206
	ds_read_b128 v[226:229], v126
	ds_read_b128 v[230:233], v126 offset:6144
	v_add_f32_e32 v126, v50, v66
	v_add_f32_e32 v127, v51, v67
	v_cvt_pk_bf16_f32 v50, v50, v51
	v_cvt_pk_bf16_f32 v51, v52, v53
	s_waitcnt lgkmcnt(5)
	v_mfma_f32_32x32x16_bf16 v[98:113], v[210:213], v[130:133], v[98:113]
	v_add_f32_e64 v210, v52, v68
	v_add_f32_e64 v211, v53, v69
	v_cvt_pk_bf16_f32 v52, v54, v55
	v_cvt_pk_bf16_f32 v53, v56, v57
	v_add_f32_e64 v126, v210, v126
	v_add_f32_e64 v127, v211, v127
	v_add_f32_e64 v210, v54, v70
	v_add_f32_e64 v211, v55, v71
	v_cvt_pk_bf16_f32 v54, v58, v59
	s_waitcnt lgkmcnt(4)
	v_mfma_f32_32x32x16_bf16 v[82:97], v[218:221], v[130:133], v[82:97]
	v_add_f32_e64 v126, v210, v126
	v_add_f32_e64 v127, v211, v127
	v_add_f32_e64 v210, v56, v72
	v_add_f32_e64 v211, v57, v73
	v_cvt_pk_bf16_f32 v55, v60, v61
	v_cvt_pk_bf16_f32 v56, v62, v63
	v_cvt_pk_bf16_f32 v57, v64, v65
	v_add_f32_e64 v126, v210, v126
	v_add_f32_e64 v127, v211, v127
	v_add_f32_e32 v210, v58, v74
	v_add_f32_e32 v211, v59, v75
	v_cvt_pk_bf16_f32 v58, v66, v67
	v_cvt_pk_bf16_f32 v59, v68, v69
	s_waitcnt lgkmcnt(3)
	v_mfma_f32_32x32x16_bf16 v[98:113], v[214:217], v[146:149], v[98:113]
	v_add_f32_e64 v126, v210, v126
	v_add_f32_e64 v127, v211, v127
	v_add_f32_e64 v210, v60, v76
	v_add_f32_e64 v211, v61, v77
	v_cvt_pk_bf16_f32 v60, v70, v71
	v_cvt_pk_bf16_f32 v61, v72, v73
	v_add_f32_e64 v126, v210, v126
	v_add_f32_e64 v127, v211, v127
	v_add_f32_e32 v210, v62, v78
	v_add_f32_e32 v211, v63, v79
	v_cvt_pk_bf16_f32 v62, v74, v75
	v_cvt_pk_bf16_f32 v63, v76, v77
	s_waitcnt lgkmcnt(2)
; DEVI void pv_both(f32x16& o0, f32x16& o1, int vb, bf16x8 pa0, bf16x8 pa1, bf16x8 pa2, bf16x8 pa3) {
;     const s16x4 a0 = tr_read<v_rd_off(0, 0, 0)>(vb), b0 = tr_read<v_rd_off(0, 0, 1)>(vb), a1 = tr_read<v_rd_off(0, 1, 0)>(vb), b1 = tr_read<v_rd_off(0, 1, 1)>(vb);
;     const s16x4 a2 = tr_read<v_rd_off(0, 2, 0)>(vb), b2 = tr_read<v_rd_off(0, 2, 1)>(vb), a3 = tr_read<v_rd_off(0, 3, 0)>(vb), b3 = tr_read<v_rd_off(0, 3, 1)>(vb);
;     const s16x4 c0 = tr_read<v_rd_off(1, 0, 0)>(vb), d0 = tr_read<v_rd_off(1, 0, 1)>(vb), c1 = tr_read<v_rd_off(1, 1, 0)>(vb), d1 = tr_read<v_rd_off(1, 1, 1)>(vb);
;     const s16x4 c2 = tr_read<v_rd_off(1, 2, 0)>(vb), d2 = tr_read<v_rd_off(1, 2, 1)>(vb), c3 = tr_read<v_rd_off(1, 3, 0)>(vb), d3 = tr_read<v_rd_off(1, 3, 1)>(vb);
;     asm volatile("s_waitcnt lgkmcnt(8)" ::: "memory"); SBAR();
;     ...
;     o0 = __builtin_amdgcn_mfma_f32_32x32x16_bf16(pa0, PK(a0, b0), o0, 0, 0, 0);
;     o0 = __builtin_amdgcn_mfma_f32_32x32x16_bf16(pa1, PK(a1, b1), o0, 0, 0, 0);
;     o0 = __builtin_amdgcn_mfma_f32_32x32x16_bf16(pa2, PK(a2, b2), o0, 0, 0, 0);
;     o0 = __builtin_amdgcn_mfma_f32_32x32x16_bf16(pa3, PK(a3, b3), o0, 0, 0, 0);
;     asm volatile("s_waitcnt lgkmcnt(0)" ::: "memory"); SBAR();
;     o1 = __builtin_amdgcn_mfma_f32_32x32x16_bf16(pa0, PK(c0, d0), o1, 0, 0, 0);
;     o1 = __builtin_amdgcn_mfma_f32_32x32x16_bf16(pa1, PK(c1, d1), o1, 0, 0, 0);
;     o1 = __builtin_amdgcn_mfma_f32_32x32x16_bf16(pa2, PK(c2, d2), o1, 0, 0, 0);
;     o1 = __builtin_amdgcn_mfma_f32_32x32x16_bf16(pa3, PK(c3, d3), o1, 0, 0, 0);
;     ...
; }
; template <bool FIRST> DEVI bool partialSM(f32x16& p0, f32x16& p1, float& m_reg, float& alpha) {
;     float pmax = p0[0];
; #pragma unroll
;     for (int r = 1; r < 16; ++r) pmax = fmaxf(pmax, p0[r]);
; #pragma unroll
;     for (int r = 0; r < 16; ++r) pmax = fmaxf(pmax, p1[r]);
;     { auto rr = __builtin_amdgcn_permlane32_swap(__float_as_uint(pmax), __float_as_uint(pmax), false, false);
;       pmax = fmaxf(__uint_as_float(rr[0]), __uint_as_float(rr[1])); }
;     if (FIRST) { m_reg = pmax; alpha = 1.f;
; #pragma unroll
;         for (int r = 0; r < 16; ++r) { p0[r] = __builtin_amdgcn_exp2f(p0[r] - pmax); p1[r] = p1[r] - pmax; }
;         return false;
;     } else if (__builtin_expect(__all(pmax <= ATT_THR), 1)) { alpha = 1.f;
; #pragma unroll
;         for (int r = 0; r < 16; ++r) p0[r] = __builtin_amdgcn_exp2f(p0[r]);
	v_mfma_f32_32x32x16_bf16 v[82:97], v[222:225], v[146:149], v[82:97]
	v_add_f32_e64 v126, v210, v126
	v_add_f32_e64 v127, v211, v127
	v_add_f32_e64 v210, v64, v80
	v_add_f32_e64 v211, v65, v81
	v_cvt_pk_bf16_f32 v64, v78, v79
	v_cvt_pk_bf16_f32 v65, v80, v81
	ds_read_b64_tr_b16 v[66:67], v174 offset:0
	ds_read_b64_tr_b16 v[68:69], v174 offset:0x400
	ds_read_b64_tr_b16 v[70:71], v174 offset:0x800
	ds_read_b64_tr_b16 v[72:73], v174 offset:0xc00
	ds_read_b64_tr_b16 v[74:75], v174 offset:0x1000
	ds_read_b64_tr_b16 v[76:77], v174 offset:0x1400
	ds_read_b64_tr_b16 v[78:79], v174 offset:0x1800
	ds_read_b64_tr_b16 v[80:81], v174 offset:0x1c00
	v_add_f32_e64 v126, v210, v126
	v_add_f32_e64 v127, v211, v127
	ds_read_b64_tr_b16 v[210:211], v174 offset:0x200
	ds_read_b64_tr_b16 v[212:213], v174 offset:0x600
	ds_read_b64_tr_b16 v[214:215], v174 offset:0xa00
	s_waitcnt lgkmcnt(12)
	v_mfma_f32_32x32x16_bf16 v[98:113], v[226:229], v[142:145], v[98:113]
	ds_read_b64_tr_b16 v[216:217], v174 offset:0xe00
	ds_read_b64_tr_b16 v[218:219], v174 offset:0x1200
	ds_read_b64_tr_b16 v[220:221], v174 offset:0x1600
	ds_read_b64_tr_b16 v[222:223], v174 offset:0x1a00
	ds_read_b64_tr_b16 v[224:225], v174 offset:0x1e00
	v_add_f32_e32 v126, v126, v127
	s_waitcnt lgkmcnt(15)
	v_mfma_f32_32x32x16_bf16 v[82:97], v[230:233], v[142:145], v[82:97]
	v_mov_b32_e32 v127, v126
	s_nop 1
	v_permlane32_swap_b32_e32 v126, v127
	s_waitcnt lgkmcnt(14)
	v_mfma_f32_32x32x16_bf16 v[18:33], v[50:53], v[66:69], v[18:33]
	s_waitcnt lgkmcnt(6)
	v_mfma_f32_32x32x16_bf16 v[2:17], v[50:53], v[210:213], v[2:17]
	s_nop 4
	v_max_f32_e32 v249, v99, v99
	v_max_f32_e32 v250, v98, v98
	v_max_f32_e32 v249, v250, v249
	v_max3_f32 v249, v249, v100, v101
	v_max3_f32 v249, v249, v102, v103
	v_max3_f32 v251, v249, v104, v105
	v_max3_f32 v251, v251, v106, v107
	v_exp_f32_e32 v50, v98
	v_exp_f32_e32 v51, v99
	v_exp_f32_e32 v52, v100
	v_exp_f32_e32 v53, v101
	v_mov_b64_e32 v[66:67], v[82:83]
	v_mov_b64_e32 v[68:69], v[84:85]
	v_mfma_f32_32x32x16_bf16 v[18:33], v[54:57], v[70:73], v[18:33]
	s_waitcnt lgkmcnt(4)
	v_mfma_f32_32x32x16_bf16 v[2:17], v[54:57], v[214:217], v[2:17]
	v_max3_f32 v251, v251, v108, v109
	v_max3_f32 v251, v251, v110, v111
	v_max3_f32 v251, v251, v112, v113
	v_max3_f32 v251, v251, v82, v83
	v_max3_f32 v251, v251, v84, v85
	v_max3_f32 v251, v251, v86, v87
	v_max3_f32 v251, v251, v88, v89
	v_exp_f32_e32 v54, v102
	v_exp_f32_e32 v55, v103
	v_exp_f32_e32 v56, v104
	v_exp_f32_e32 v57, v105
	v_mov_b64_e32 v[70:71], v[86:87]
	v_mov_b64_e32 v[72:73], v[88:89]
	v_mfma_f32_32x32x16_bf16 v[18:33], v[58:61], v[74:77], v[18:33]
	s_waitcnt lgkmcnt(2)
	v_mfma_f32_32x32x16_bf16 v[2:17], v[58:61], v[218:221], v[2:17]
	v_max3_f32 v251, v251, v90, v91
	v_max3_f32 v251, v251, v92, v93
	v_max3_f32 v251, v251, v94, v95
	v_max3_f32 v251, v251, v96, v97
	v_mov_b32_e32 v252, v251
	s_nop 1
	v_permlane32_swap_b32_e32 v251, v252
	v_exp_f32_e32 v58, v106
	v_exp_f32_e32 v59, v107
	v_exp_f32_e32 v60, v108
	v_exp_f32_e32 v61, v109
	v_mov_b64_e32 v[74:75], v[90:91]
	v_mov_b64_e32 v[76:77], v[92:93]
	v_mfma_f32_32x32x16_bf16 v[18:33], v[62:65], v[78:81], v[18:33]
	s_waitcnt lgkmcnt(0)
	v_mfma_f32_32x32x16_bf16 v[2:17], v[62:65], v[222:225], v[2:17]
	v_exp_f32_e32 v62, v110
	v_exp_f32_e32 v63, v111
	v_exp_f32_e32 v64, v112
	v_exp_f32_e32 v65, v113
	v_mov_b64_e32 v[78:79], v[94:95]
	v_mov_b64_e32 v[80:81], v[96:97]
	v_max_f32_e32 v252, v252, v252
	v_max_f32_e32 v251, v251, v251
	v_max_f32_e32 v174, v251, v252
	v_cmp_ge_f32_e32 vcc, s79, v174
	s_cmp_lg_u64 vcc, exec
	s_cselect_b64 s[6:7], -1, 0
	s_cbranch_scc1 .LBB0_711
	v_mov_b32_e32 v202, 1.0
	v_mov_b32_e32 v203, v209
	s_branch .LBB0_716

; template <bool FIRST> DEVI bool partialSM(f32x16& p0, f32x16& p1, float& m_reg, float& alpha) {
;     float pmax = p0[0];
; #pragma unroll
;     for (int r = 1; r < 16; ++r) pmax = fmaxf(pmax, p0[r]);
; #pragma unroll
;     for (int r = 0; r < 16; ++r) pmax = fmaxf(pmax, p1[r]);
;     { auto rr = __builtin_amdgcn_permlane32_swap(__float_as_uint(pmax), __float_as_uint(pmax), false, false);
;       pmax = fmaxf(__uint_as_float(rr[0]), __uint_as_float(rr[1])); }
;     if (FIRST) { m_reg = pmax; alpha = 1.f;
; #pragma unroll
;         for (int r = 0; r < 16; ++r) { p0[r] = __builtin_amdgcn_exp2f(p0[r] - pmax); p1[r] = p1[r] - pmax; }
;         return false;
;     } else if (__builtin_expect(__all(pmax <= ATT_THR), 1)) { alpha = 1.f;
; #pragma unroll
;         for (int r = 0; r < 16; ++r) p0[r] = __builtin_amdgcn_exp2f(p0[r]);
;         return false;
;     } else { const float d = fmaxf(pmax, 0.f); alpha = __builtin_amdgcn_exp2f(-d); m_reg += d;
; #pragma unroll
;         for (int r = 0; r < 16; ++r) { p0[r] = __builtin_amdgcn_exp2f(p0[r] - d); p1[r] = p1[r] - d; }
;         return true;
;     }
; }
; DEVI void finishSM(f32x16& p0, f32x16& p1, float alpha, float& l_reg, bf16x8& pa0, bf16x8& pa1, bf16x8& pa2, bf16x8& pa3) {
; #pragma unroll
;     for (int r = 0; r < 16; ++r) p1[r] = __builtin_amdgcn_exp2f(p1[r]);
;     f32x2 s2 = (f32x2){p0[0], p0[1]} + (f32x2){p1[0], p1[1]};
; #pragma unroll
;     for (int r = 2; r < 16; r += 2) s2 += (f32x2){p0[r], p0[r + 1]} + (f32x2){p1[r], p1[r + 1]};
;     float ps = s2[0] + s2[1];
;     { auto rr = __builtin_amdgcn_permlane32_swap(__float_as_uint(ps), __float_as_uint(ps), false, false);
;       ps = __uint_as_float(rr[0]) + __uint_as_float(rr[1]); }
;     l_reg = l_reg * alpha + ps;
;     ...
;     PK4(p0, 0, pa0); PK4(p0, 8, pa1); PK4(p1, 0, pa2); PK4(p1, 8, pa3);
;     ...
; }
; DEVI void qkt(f32x16& p0, f32x16& p1, const char* Kb, const bf16x8 (&qr)[6], int r32, int hi, const f32x16& cinit) {
; #pragma unroll
;     for (int d0 = 0; d0 < 6; ++d0) { const int cb = (d0 * 16 + hi * 8) * 2;
;         const bf16x8 k0 = *(const bf16x8*)(Kb + KSWZ(r32, cb)), k1 = *(const bf16x8*)(Kb + KSWZ(32 + r32, cb));
;         p0 = __builtin_amdgcn_mfma_f32_32x32x16_bf16(k0, qr[d0], d0 == 0 ? cinit : p0, 0, 0, 0);
;         p1 = __builtin_amdgcn_mfma_f32_32x32x16_bf16(k1, qr[d0], d0 == 0 ? cinit : p1, 0, 0, 0); }
; }
.LBB0_2260:
	v_add_u32_e32 v174, s98, v205
	v_exp_f32_e32 v66, v66
	v_exp_f32_e32 v67, v67
	s_waitcnt lgkmcnt(1)
	v_mfma_f32_32x32x16_bf16 v[98:113], v[82:85], v[150:153], v[34:49]
	v_add_u32_e32 v82, s98, v184
	v_add_u32_e32 v83, s98, v185
	ds_read_b128 v[210:213], v82 offset:12288
	ds_read_b128 v[214:217], v82 offset:18432
	ds_read_b128 v[218:221], v83 offset:12288
	ds_read_b128 v[222:225], v83 offset:18432
	v_exp_f32_e32 v68, v68
	v_exp_f32_e32 v69, v69
	v_exp_f32_e32 v70, v70
	v_exp_f32_e32 v71, v71
	s_waitcnt lgkmcnt(4)
	v_mfma_f32_32x32x16_bf16 v[82:97], v[124:127], v[150:153], v[34:49]
	ds_read_b128 v[124:127], v174 offset:12288
	ds_read_b128 v[226:229], v174 offset:18432
	v_exp_f32_e32 v72, v72
	v_exp_f32_e32 v73, v73
	v_exp_f32_e32 v74, v74
	v_exp_f32_e32 v75, v75
	v_exp_f32_e32 v76, v76
	v_exp_f32_e32 v77, v77
	s_waitcnt lgkmcnt(5)
	v_mfma_f32_32x32x16_bf16 v[98:113], v[210:213], v[138:141], v[98:113]
	v_add_u32_e32 v174, s98, v206
	v_exp_f32_e32 v78, v78
	v_exp_f32_e32 v79, v79
	ds_read_b128 v[230:233], v174 offset:12288
	ds_read_b128 v[234:237], v174 offset:18432
	v_exp_f32_e32 v80, v80
	v_exp_f32_e32 v81, v81
	v_add_u32_e32 v174, s98, v207
	s_waitcnt lgkmcnt(6)
	v_mfma_f32_32x32x16_bf16 v[82:97], v[214:217], v[138:141], v[82:97]
	v_add_f32_e64 v214, v50, v66
	v_add_f32_e64 v215, v51, v67
	v_add_f32_e64 v216, v52, v68
	v_add_f32_e64 v217, v53, v69
	v_lshl_add_u32 v203, s71, 14, v115
	v_add_f32_e32 v214, v216, v214
	v_add_f32_e32 v215, v217, v215
	v_add_f32_e32 v216, v54, v70
	v_add_f32_e32 v217, v55, v71
	ds_read_b128 v[210:213], v174 offset:12288
	ds_read_b128 v[238:241], v174 offset:18432
	v_add_f32_e32 v214, v216, v214
	v_add_f32_e32 v215, v217, v215
	s_waitcnt lgkmcnt(7)
	v_mfma_f32_32x32x16_bf16 v[98:113], v[218:221], v[134:137], v[98:113]
	v_add_f32_e64 v216, v56, v72
	v_add_f32_e64 v217, v57, v73
	v_cvt_pk_bf16_f32 v50, v50, v51
	v_cvt_pk_bf16_f32 v51, v52, v53
	v_cvt_pk_bf16_f32 v52, v54, v55
	v_cvt_pk_bf16_f32 v53, v56, v57
	v_cvt_pk_bf16_f32 v54, v58, v59
	v_add_f32_e64 v214, v216, v214
	v_add_f32_e64 v215, v217, v215
	s_waitcnt lgkmcnt(6)
	v_mfma_f32_32x32x16_bf16 v[82:97], v[222:225], v[134:137], v[82:97]
	v_add_f32_e64 v216, v58, v74
	v_add_f32_e64 v217, v59, v75
	v_cvt_pk_bf16_f32 v55, v60, v61
	v_cvt_pk_bf16_f32 v56, v62, v63
	v_cvt_pk_bf16_f32 v57, v64, v65
	v_cvt_pk_bf16_f32 v58, v66, v67
	v_cvt_pk_bf16_f32 v59, v68, v69
	v_add_f32_e64 v214, v216, v214
	v_add_f32_e64 v215, v217, v215
	s_waitcnt lgkmcnt(5)
	v_mfma_f32_32x32x16_bf16 v[98:113], v[124:127], v[130:133], v[98:113]
	v_add_f32_e64 v216, v60, v76
	v_add_f32_e64 v217, v61, v77
	v_add_f32_e64 v126, v62, v78
	v_add_f32_e64 v127, v63, v79
	v_add_f32_e64 v124, v216, v214
	v_add_f32_e64 v125, v217, v215
	v_cvt_pk_bf16_f32 v60, v70, v71
	v_cvt_pk_bf16_f32 v61, v72, v73
	v_cvt_pk_bf16_f32 v62, v74, v75
	v_cvt_pk_bf16_f32 v63, v76, v77
	s_waitcnt lgkmcnt(4)
	v_mfma_f32_32x32x16_bf16 v[82:97], v[226:229], v[130:133], v[82:97]
	v_add_f32_e64 v124, v126, v124
	v_add_f32_e64 v125, v127, v125
	v_add_f32_e64 v126, v64, v80
	v_add_f32_e64 v127, v65, v81
	v_cvt_pk_bf16_f32 v64, v78, v79
	v_cvt_pk_bf16_f32 v65, v80, v81
	ds_read_b64_tr_b16 v[66:67], v203 offset:0
	ds_read_b64_tr_b16 v[68:69], v203 offset:0x400
	ds_read_b64_tr_b16 v[70:71], v203 offset:0x800
	s_waitcnt lgkmcnt(6)
	v_mfma_f32_32x32x16_bf16 v[98:113], v[230:233], v[146:149], v[98:113]
	ds_read_b64_tr_b16 v[72:73], v203 offset:0xc00
	ds_read_b64_tr_b16 v[74:75], v203 offset:0x1000
	ds_read_b64_tr_b16 v[76:77], v203 offset:0x1400
	ds_read_b64_tr_b16 v[78:79], v203 offset:0x1800
	ds_read_b64_tr_b16 v[80:81], v203 offset:0x1c00
	v_add_f32_e64 v124, v126, v124
	v_add_f32_e64 v125, v127, v125
	s_waitcnt lgkmcnt(10)
	v_mfma_f32_32x32x16_bf16 v[82:97], v[234:237], v[146:149], v[82:97]
	v_add_f32_e32 v124, v124, v125
	s_nop 0
	v_mov_b32_e32 v125, v124
	s_nop 1
	v_permlane32_swap_b32_e32 v124, v125
	s_waitcnt lgkmcnt(9)
	v_mfma_f32_32x32x16_bf16 v[98:113], v[210:213], v[142:145], v[98:113]
	ds_read_b64_tr_b16 v[210:211], v203 offset:0x200
	ds_read_b64_tr_b16 v[212:213], v203 offset:0x600
	ds_read_b64_tr_b16 v[214:215], v203 offset:0xa00
	ds_read_b64_tr_b16 v[216:217], v203 offset:0xe00
	ds_read_b64_tr_b16 v[218:219], v203 offset:0x1200
	ds_read_b64_tr_b16 v[220:221], v203 offset:0x1600
	ds_read_b64_tr_b16 v[222:223], v203 offset:0x1a00
	s_waitcnt lgkmcnt(15)
	v_mfma_f32_32x32x16_bf16 v[82:97], v[238:241], v[142:145], v[82:97]
	ds_read_b64_tr_b16 v[224:225], v203 offset:0x1e00
	s_waitcnt lgkmcnt(14)
	v_mfma_f32_32x32x16_bf16 v[18:33], v[50:53], v[66:69], v[18:33]
	s_waitcnt lgkmcnt(6)
	v_mfma_f32_32x32x16_bf16 v[2:17], v[50:53], v[210:213], v[2:17]
	s_nop 8
	v_max_f32_e32 v249, v99, v99
	v_max_f32_e32 v250, v98, v98
	v_max_f32_e32 v249, v250, v249
	v_max3_f32 v249, v249, v100, v101
	v_max3_f32 v249, v249, v102, v103
	v_max3_f32 v251, v249, v104, v105
	v_max3_f32 v251, v251, v106, v107
	v_exp_f32_e32 v50, v98
	v_exp_f32_e32 v51, v99
	v_exp_f32_e32 v52, v100
	v_exp_f32_e32 v53, v101
	v_mov_b64_e32 v[66:67], v[82:83]
	v_mov_b64_e32 v[68:69], v[84:85]
	v_mfma_f32_32x32x16_bf16 v[18:33], v[54:57], v[70:73], v[18:33]
	s_waitcnt lgkmcnt(4)
	v_mfma_f32_32x32x16_bf16 v[2:17], v[54:57], v[214:217], v[2:17]
	v_max3_f32 v251, v251, v108, v109
	v_max3_f32 v251, v251, v110, v111
	v_max3_f32 v251, v251, v112, v113
	v_max3_f32 v251, v251, v82, v83
	v_max3_f32 v251, v251, v84, v85
	v_max3_f32 v251, v251, v86, v87
	v_max3_f32 v251, v251, v88, v89
	v_exp_f32_e32 v54, v102
	v_exp_f32_e32 v55, v103
	v_exp_f32_e32 v56, v104
	v_exp_f32_e32 v57, v105
	v_mov_b64_e32 v[70:71], v[86:87]
	v_mov_b64_e32 v[72:73], v[88:89]
	v_mfma_f32_32x32x16_bf16 v[18:33], v[58:61], v[74:77], v[18:33]
	s_waitcnt lgkmcnt(2)
	v_mfma_f32_32x32x16_bf16 v[2:17], v[58:61], v[218:221], v[2:17]
	v_max3_f32 v251, v251, v90, v91
	v_max3_f32 v251, v251, v92, v93
	v_max3_f32 v251, v251, v94, v95
	v_max3_f32 v251, v251, v96, v97
	v_mov_b32_e32 v252, v251
	s_nop 1
	v_permlane32_swap_b32_e32 v251, v252
	v_exp_f32_e32 v58, v106
	v_exp_f32_e32 v59, v107
	v_exp_f32_e32 v60, v108
	v_exp_f32_e32 v61, v109
	v_mov_b64_e32 v[74:75], v[90:91]
	v_mov_b64_e32 v[76:77], v[92:93]
	v_mfma_f32_32x32x16_bf16 v[18:33], v[62:65], v[78:81], v[18:33]
	s_waitcnt lgkmcnt(0)
	v_mfma_f32_32x32x16_bf16 v[2:17], v[62:65], v[222:225], v[2:17]
	v_exp_f32_e32 v62, v110
	v_exp_f32_e32 v63, v111
	v_exp_f32_e32 v64, v112
	v_exp_f32_e32 v65, v113
	v_mov_b64_e32 v[78:79], v[94:95]
	v_mov_b64_e32 v[80:81], v[96:97]
	v_max_f32_e32 v252, v252, v252
	v_max_f32_e32 v251, v251, v251
	v_max_f32_e32 v126, v251, v252
	v_cmp_ge_f32_e32 vcc, s80, v126
	s_cmp_lg_u64 vcc, exec
	s_cselect_b64 s[6:7], -1, 0
	s_cbranch_scc1 .LBB0_2269
	v_mov_b32_e32 v209, 1.0
	v_mov_b32_e32 v210, v204
	s_branch .LBB0_2263

; #define PK4(P, BASE, OUT) do { u32x4 w = {cvt_pk_bf16(P[BASE + 0], P[BASE + 1]), cvt_pk_bf16(P[BASE + 2], P[BASE + 3]), cvt_pk_bf16(P[BASE + 4], P[BASE + 5]), cvt_pk_bf16(P[BASE + 6], P[BASE + 7])}; \
;     OUT = *reinterpret_cast<bf16x8*>(&w); } while (0)
; DEVI void finishSM(f32x16& p0, f32x16& p1, float alpha, float& l_reg, bf16x8& pa0, bf16x8& pa1, bf16x8& pa2, bf16x8& pa3) {
; #pragma unroll
;     for (int r = 0; r < 16; ++r) p1[r] = __builtin_amdgcn_exp2f(p1[r]);
;     f32x2 s2 = (f32x2){p0[0], p0[1]} + (f32x2){p1[0], p1[1]};
; #pragma unroll
;     for (int r = 2; r < 16; r += 2) s2 += (f32x2){p0[r], p0[r + 1]} + (f32x2){p1[r], p1[r + 1]};
;     float ps = s2[0] + s2[1];
;     { auto rr = __builtin_amdgcn_permlane32_swap(__float_as_uint(ps), __float_as_uint(ps), false, false);
;       ps = __uint_as_float(rr[0]) + __uint_as_float(rr[1]); }
;     l_reg = l_reg * alpha + ps;
;     ...
;     PK4(p0, 0, pa0); PK4(p0, 8, pa1); PK4(p1, 0, pa2); PK4(p1, 8, pa3);
;     ...
; }
; DEVI void qkt(f32x16& p0, f32x16& p1, const char* Kb, const bf16x8 (&qr)[6], int r32, int hi, const f32x16& cinit) {
; #pragma unroll
;     for (int d0 = 0; d0 < 6; ++d0) { const int cb = (d0 * 16 + hi * 8) * 2;
;         const bf16x8 k0 = *(const bf16x8*)(Kb + KSWZ(r32, cb)), k1 = *(const bf16x8*)(Kb + KSWZ(32 + r32, cb));
;         p0 = __builtin_amdgcn_mfma_f32_32x32x16_bf16(k0, qr[d0], d0 == 0 ? cinit : p0, 0, 0, 0);
;         p1 = __builtin_amdgcn_mfma_f32_32x32x16_bf16(k1, qr[d0], d0 == 0 ? cinit : p1, 0, 0, 0); }
; }
.LBB0_2266:
	s_mul_i32 s98, s61, 0x6000
	s_add_i32 s98, s96, s98
	s_lshl_b32 s99, s61, 14
	s_add_i32 s99, s97, s99
	s_mul_i32 s6, s2, 0x6000
	s_add_i32 s6, s6, 0
	v_add_u32_e32 v86, s6, v129
	v_lshl_add_u64 v[250:251], v[118:119], 0, s[12:13]
	s_mov_b32 m0, s98
	s_barrier
	ds_read_b128 v[82:85], v86
	ds_read_b128 v[212:215], v86 offset:6144
	global_load_lds_dwordx4 v[250:251], off
	v_exp_f32_e32 v66, v66
	s_waitcnt lgkmcnt(1)
	v_mfma_f32_32x32x16_bf16 v[98:113], v[82:85], v[150:153], v[34:49]
	v_add_u32_e32 v126, s6, v184
	v_lshl_add_u64 v[250:251], v[120:121], 0, s[12:13]
	s_add_i32 m0, s98, 0x2000
	v_exp_f32_e32 v67, v67
	v_exp_f32_e32 v68, v68
	global_load_lds_dwordx4 v[250:251], off
	v_exp_f32_e32 v69, v69
	v_exp_f32_e32 v70, v70
	v_exp_f32_e32 v71, v71
	v_exp_f32_e32 v72, v72
	s_waitcnt lgkmcnt(0)
	v_mfma_f32_32x32x16_bf16 v[82:97], v[212:215], v[150:153], v[34:49]
	ds_read_b128 v[212:215], v126
	ds_read_b128 v[216:219], v126 offset:6144
	v_add_u32_e32 v126, s6, v185
	v_lshl_add_u64 v[250:251], v[122:123], 0, s[12:13]
	s_add_i32 m0, s98, 0x4000
	v_exp_f32_e32 v73, v73
	v_exp_f32_e32 v74, v74
	global_load_lds_dwordx4 v[250:251], off
	v_exp_f32_e32 v75, v75
	v_exp_f32_e32 v76, v76
	v_exp_f32_e32 v77, v77
	s_waitcnt lgkmcnt(1)
	v_mfma_f32_32x32x16_bf16 v[98:113], v[212:215], v[138:141], v[98:113]
	s_mov_b32 m0, s99
	v_exp_f32_e32 v78, v78
	v_exp_f32_e32 v79, v79
	v_lshl_add_u64 v[250:251], v[116:117], 0, s[40:41]
	global_load_lds_dwordx4 v[116:117], off
	s_add_i32 m0, s99, 0x2000
	v_exp_f32_e32 v80, v80
	v_exp_f32_e32 v81, v81
	v_add_u32_e32 v174, 0x2000, v203
	global_load_lds_dwordx4 v[250:251], off
	s_waitcnt lgkmcnt(0)
	v_mfma_f32_32x32x16_bf16 v[82:97], v[216:219], v[138:141], v[82:97]
	ds_read_b128 v[212:215], v126
	ds_read_b128 v[216:219], v126 offset:6144
	v_add_u32_e32 v126, s6, v205
	s_waitcnt lgkmcnt(1)
	v_mfma_f32_32x32x16_bf16 v[98:113], v[212:215], v[134:137], v[98:113]
	ds_read_b128 v[212:215], v126
	ds_read_b128 v[220:223], v126 offset:6144
	v_add_u32_e32 v126, s6, v206
	s_waitcnt lgkmcnt(2)
	v_mfma_f32_32x32x16_bf16 v[82:97], v[216:219], v[134:137], v[82:97]
	ds_read_b128 v[216:219], v126
	ds_read_b128 v[224:227], v126 offset:6144
	v_add_u32_e32 v126, s6, v207
	ds_read_b128 v[228:231], v126
	ds_read_b128 v[232:235], v126 offset:6144
	v_add_f32_e32 v126, v50, v66
	v_add_f32_e32 v127, v51, v67
	v_cvt_pk_bf16_f32 v50, v50, v51
	v_cvt_pk_bf16_f32 v51, v52, v53
	s_waitcnt lgkmcnt(5)
	v_mfma_f32_32x32x16_bf16 v[98:113], v[212:215], v[130:133], v[98:113]
	v_add_f32_e64 v212, v52, v68
	v_add_f32_e64 v213, v53, v69
	v_cvt_pk_bf16_f32 v52, v54, v55
	v_cvt_pk_bf16_f32 v53, v56, v57
	v_add_f32_e64 v126, v212, v126
	v_add_f32_e64 v127, v213, v127
	v_add_f32_e64 v212, v54, v70
	v_add_f32_e64 v213, v55, v71
	v_cvt_pk_bf16_f32 v54, v58, v59
	s_waitcnt lgkmcnt(4)
	v_mfma_f32_32x32x16_bf16 v[82:97], v[220:223], v[130:133], v[82:97]
	v_add_f32_e64 v126, v212, v126
	v_add_f32_e64 v127, v213, v127
	v_add_f32_e64 v212, v56, v72
	v_add_f32_e64 v213, v57, v73
	v_cvt_pk_bf16_f32 v55, v60, v61
	v_cvt_pk_bf16_f32 v56, v62, v63
	v_cvt_pk_bf16_f32 v57, v64, v65
	v_add_f32_e64 v126, v212, v126
	v_add_f32_e64 v127, v213, v127
	v_add_f32_e32 v212, v58, v74
	v_add_f32_e32 v213, v59, v75
	v_cvt_pk_bf16_f32 v58, v66, v67
	v_cvt_pk_bf16_f32 v59, v68, v69
	s_waitcnt lgkmcnt(3)
	v_mfma_f32_32x32x16_bf16 v[98:113], v[216:219], v[146:149], v[98:113]
	v_add_f32_e64 v126, v212, v126
	v_add_f32_e64 v127, v213, v127
	v_add_f32_e64 v212, v60, v76
	v_add_f32_e64 v213, v61, v77
	v_cvt_pk_bf16_f32 v60, v70, v71
	v_cvt_pk_bf16_f32 v61, v72, v73
	v_add_f32_e64 v126, v212, v126
	v_add_f32_e64 v127, v213, v127
	v_add_f32_e32 v212, v62, v78
	v_add_f32_e32 v213, v63, v79
	v_cvt_pk_bf16_f32 v62, v74, v75
	v_cvt_pk_bf16_f32 v63, v76, v77
	s_waitcnt lgkmcnt(2)
; DEVI void pv_both(f32x16& o0, f32x16& o1, int vb, bf16x8 pa0, bf16x8 pa1, bf16x8 pa2, bf16x8 pa3) {
;     const s16x4 a0 = tr_read<v_rd_off(0, 0, 0)>(vb), b0 = tr_read<v_rd_off(0, 0, 1)>(vb), a1 = tr_read<v_rd_off(0, 1, 0)>(vb), b1 = tr_read<v_rd_off(0, 1, 1)>(vb);
;     const s16x4 a2 = tr_read<v_rd_off(0, 2, 0)>(vb), b2 = tr_read<v_rd_off(0, 2, 1)>(vb), a3 = tr_read<v_rd_off(0, 3, 0)>(vb), b3 = tr_read<v_rd_off(0, 3, 1)>(vb);
;     const s16x4 c0 = tr_read<v_rd_off(1, 0, 0)>(vb), d0 = tr_read<v_rd_off(1, 0, 1)>(vb), c1 = tr_read<v_rd_off(1, 1, 0)>(vb), d1 = tr_read<v_rd_off(1, 1, 1)>(vb);
;     const s16x4 c2 = tr_read<v_rd_off(1, 2, 0)>(vb), d2 = tr_read<v_rd_off(1, 2, 1)>(vb), c3 = tr_read<v_rd_off(1, 3, 0)>(vb), d3 = tr_read<v_rd_off(1, 3, 1)>(vb);
;     asm volatile("s_waitcnt lgkmcnt(8)" ::: "memory"); SBAR();
;     ...
;     o0 = __builtin_amdgcn_mfma_f32_32x32x16_bf16(pa0, PK(a0, b0), o0, 0, 0, 0);
;     o0 = __builtin_amdgcn_mfma_f32_32x32x16_bf16(pa1, PK(a1, b1), o0, 0, 0, 0);
;     o0 = __builtin_amdgcn_mfma_f32_32x32x16_bf16(pa2, PK(a2, b2), o0, 0, 0, 0);
;     o0 = __builtin_amdgcn_mfma_f32_32x32x16_bf16(pa3, PK(a3, b3), o0, 0, 0, 0);
;     asm volatile("s_waitcnt lgkmcnt(0)" ::: "memory"); SBAR();
;     o1 = __builtin_amdgcn_mfma_f32_32x32x16_bf16(pa0, PK(c0, d0), o1, 0, 0, 0);
;     o1 = __builtin_amdgcn_mfma_f32_32x32x16_bf16(pa1, PK(c1, d1), o1, 0, 0, 0);
;     o1 = __builtin_amdgcn_mfma_f32_32x32x16_bf16(pa2, PK(c2, d2), o1, 0, 0, 0);
;     o1 = __builtin_amdgcn_mfma_f32_32x32x16_bf16(pa3, PK(c3, d3), o1, 0, 0, 0);
;     ...
; }
; template <bool FIRST> DEVI bool partialSM(f32x16& p0, f32x16& p1, float& m_reg, float& alpha) {
;     float pmax = p0[0];
; #pragma unroll
;     for (int r = 1; r < 16; ++r) pmax = fmaxf(pmax, p0[r]);
; #pragma unroll
;     for (int r = 0; r < 16; ++r) pmax = fmaxf(pmax, p1[r]);
;     { auto rr = __builtin_amdgcn_permlane32_swap(__float_as_uint(pmax), __float_as_uint(pmax), false, false);
;       pmax = fmaxf(__uint_as_float(rr[0]), __uint_as_float(rr[1])); }
;     if (FIRST) { m_reg = pmax; alpha = 1.f;
; #pragma unroll
;         for (int r = 0; r < 16; ++r) { p0[r] = __builtin_amdgcn_exp2f(p0[r] - pmax); p1[r] = p1[r] - pmax; }
;         return false;
;     } else if (__builtin_expect(__all(pmax <= ATT_THR), 1)) { alpha = 1.f;
; #pragma unroll
;         for (int r = 0; r < 16; ++r) p0[r] = __builtin_amdgcn_exp2f(p0[r]);
	v_mfma_f32_32x32x16_bf16 v[82:97], v[224:227], v[146:149], v[82:97]
	v_add_f32_e64 v126, v212, v126
	v_add_f32_e64 v127, v213, v127
	v_add_f32_e64 v212, v64, v80
	v_add_f32_e64 v213, v65, v81
	v_cvt_pk_bf16_f32 v64, v78, v79
	v_cvt_pk_bf16_f32 v65, v80, v81
	ds_read_b64_tr_b16 v[66:67], v174 offset:0
	ds_read_b64_tr_b16 v[68:69], v174 offset:0x400
	ds_read_b64_tr_b16 v[70:71], v174 offset:0x800
	ds_read_b64_tr_b16 v[72:73], v174 offset:0xc00
	ds_read_b64_tr_b16 v[74:75], v174 offset:0x1000
	ds_read_b64_tr_b16 v[76:77], v174 offset:0x1400
	ds_read_b64_tr_b16 v[78:79], v174 offset:0x1800
	ds_read_b64_tr_b16 v[80:81], v174 offset:0x1c00
	v_add_f32_e64 v126, v212, v126
	v_add_f32_e64 v127, v213, v127
	ds_read_b64_tr_b16 v[212:213], v174 offset:0x200
	ds_read_b64_tr_b16 v[214:215], v174 offset:0x600
	ds_read_b64_tr_b16 v[216:217], v174 offset:0xa00
	s_waitcnt lgkmcnt(12)
	v_mfma_f32_32x32x16_bf16 v[98:113], v[228:231], v[142:145], v[98:113]
	ds_read_b64_tr_b16 v[218:219], v174 offset:0xe00
	ds_read_b64_tr_b16 v[220:221], v174 offset:0x1200
	ds_read_b64_tr_b16 v[222:223], v174 offset:0x1600
	ds_read_b64_tr_b16 v[224:225], v174 offset:0x1a00
	ds_read_b64_tr_b16 v[226:227], v174 offset:0x1e00
	v_add_f32_e32 v126, v126, v127
	s_waitcnt lgkmcnt(15)
	v_mfma_f32_32x32x16_bf16 v[82:97], v[232:235], v[142:145], v[82:97]
	v_mov_b32_e32 v127, v126
	s_nop 1
	v_permlane32_swap_b32_e32 v126, v127
	s_waitcnt lgkmcnt(14)
	v_mfma_f32_32x32x16_bf16 v[18:33], v[50:53], v[66:69], v[18:33]
	s_waitcnt lgkmcnt(6)
	v_mfma_f32_32x32x16_bf16 v[2:17], v[50:53], v[212:215], v[2:17]
	s_nop 4
	v_max_f32_e32 v249, v99, v99
	v_max_f32_e32 v250, v98, v98
	v_max_f32_e32 v249, v250, v249
	v_max3_f32 v249, v249, v100, v101
	v_max3_f32 v249, v249, v102, v103
	v_max3_f32 v251, v249, v104, v105
	v_max3_f32 v251, v251, v106, v107
	v_exp_f32_e32 v50, v98
	v_exp_f32_e32 v51, v99
	v_exp_f32_e32 v52, v100
	v_exp_f32_e32 v53, v101
	v_mov_b64_e32 v[66:67], v[82:83]
	v_mov_b64_e32 v[68:69], v[84:85]
	v_mfma_f32_32x32x16_bf16 v[18:33], v[54:57], v[70:73], v[18:33]
	s_waitcnt lgkmcnt(4)
	v_mfma_f32_32x32x16_bf16 v[2:17], v[54:57], v[216:219], v[2:17]
	v_max3_f32 v251, v251, v108, v109
	v_max3_f32 v251, v251, v110, v111
	v_max3_f32 v251, v251, v112, v113
	v_max3_f32 v251, v251, v82, v83
	v_max3_f32 v251, v251, v84, v85
	v_max3_f32 v251, v251, v86, v87
	v_max3_f32 v251, v251, v88, v89
	v_exp_f32_e32 v54, v102
	v_exp_f32_e32 v55, v103
	v_exp_f32_e32 v56, v104
	v_exp_f32_e32 v57, v105
	v_mov_b64_e32 v[70:71], v[86:87]
	v_mov_b64_e32 v[72:73], v[88:89]
	v_mfma_f32_32x32x16_bf16 v[18:33], v[58:61], v[74:77], v[18:33]
	s_waitcnt lgkmcnt(2)
	v_mfma_f32_32x32x16_bf16 v[2:17], v[58:61], v[220:223], v[2:17]
	v_max3_f32 v251, v251, v90, v91
	v_max3_f32 v251, v251, v92, v93
	v_max3_f32 v251, v251, v94, v95
	v_max3_f32 v251, v251, v96, v97
	v_mov_b32_e32 v252, v251
	s_nop 1
	v_permlane32_swap_b32_e32 v251, v252
	v_exp_f32_e32 v58, v106
	v_exp_f32_e32 v59, v107
	v_exp_f32_e32 v60, v108
	v_exp_f32_e32 v61, v109
	v_mov_b64_e32 v[74:75], v[90:91]
	v_mov_b64_e32 v[76:77], v[92:93]
	v_mfma_f32_32x32x16_bf16 v[18:33], v[62:65], v[78:81], v[18:33]
	s_waitcnt lgkmcnt(0)
	v_mfma_f32_32x32x16_bf16 v[2:17], v[62:65], v[224:227], v[2:17]
	v_exp_f32_e32 v62, v110
	v_exp_f32_e32 v63, v111
	v_exp_f32_e32 v64, v112
	v_exp_f32_e32 v65, v113
	v_mov_b64_e32 v[78:79], v[94:95]
	v_mov_b64_e32 v[80:81], v[96:97]
	v_max_f32_e32 v252, v252, v252
	v_max_f32_e32 v251, v251, v251
	v_max_f32_e32 v174, v251, v252
	v_cmp_ge_f32_e32 vcc, s80, v174
	s_cmp_lg_u64 vcc, exec
	s_cselect_b64 s[6:7], -1, 0
	s_cbranch_scc1 .LBB0_2275
	v_mov_b32_e32 v203, 1.0
	v_mov_b32_e32 v204, v210
	s_branch .LBB0_2280
